# K-loops: the lgkmcnt ladder inside the MFMA groups (already satisfied by the lgkmcnt(0) in front of the barrier) and the s_nop 1 in front of the fp8 MFMA groups removed
# baseline (speedup 1.0000x reference)
.LBB0_326:
	v_add_u32_e32 v44, 0x10000, v162
	v_add_u32_e32 v168, 0x14000, v162
	ds_read_b128 v[24:27], v44
	ds_read_b128 v[28:31], v44 offset:1024
	ds_read_b128 v[40:43], v44 offset:2048
	ds_read_b128 v[44:47], v44 offset:3072
	ds_read_b128 v[146:149], v168
	ds_read_b128 v[150:153], v168 offset:1024
	ds_read_b128 v[164:167], v168 offset:2048
	ds_read_b128 v[168:171], v168 offset:3072
	s_cmp_eq_u32 s6, 28
	s_cselect_b32 s7, s54, s5
	s_cselect_b32 s8, s55, s4
	s_add_i32 s9, s5, 0xffffff80
	s_mov_b32 m0, s49
	ds_read_b128 v[172:175], v163
	ds_read_b128 v[176:179], v163 offset:1024
	ds_read_b128 v[180:183], v163 offset:2048
	ds_read_b128 v[184:187], v163 offset:3072
	ds_read_b128 v[188:191], v163 offset:4096
	ds_read_b128 v[192:195], v163 offset:5120
	ds_read_b128 v[196:199], v163 offset:6144
	ds_read_b128 v[200:203], v163 offset:7168
	buffer_load_dwordx4 v158, s[12:15], s9 offen lds
	s_mov_b32 m0, s50
	s_nop 0
	buffer_load_dwordx4 v159, s[12:15], s9 offen lds
	s_waitcnt vmcnt(8)
	s_waitcnt lgkmcnt(0)
	s_barrier
	s_setprio 1
	v_mfma_f32_16x16x32_bf16 v[136:139], v[24:27], v[172:175], v[136:139]
	v_mfma_f32_16x16x32_bf16 v[140:143], v[40:43], v[172:175], v[140:143]
	v_mfma_f32_16x16x32_bf16 v[124:127], v[24:27], v[180:183], v[124:127]
	v_mfma_f32_16x16x32_bf16 v[120:123], v[40:43], v[180:183], v[120:123]
	v_mfma_f32_16x16x32_bf16 v[108:111], v[24:27], v[188:191], v[108:111]
	v_mfma_f32_16x16x32_bf16 v[104:107], v[40:43], v[188:191], v[104:107]
	v_mfma_f32_16x16x32_bf16 v[92:95], v[24:27], v[196:199], v[92:95]
	v_mfma_f32_16x16x32_bf16 v[88:91], v[40:43], v[196:199], v[88:91]
	v_mfma_f32_16x16x32_bf16 v[136:139], v[28:31], v[176:179], v[136:139]
	v_mfma_f32_16x16x32_bf16 v[140:143], v[44:47], v[176:179], v[140:143]
	v_mfma_f32_16x16x32_bf16 v[124:127], v[28:31], v[184:187], v[124:127]
	v_mfma_f32_16x16x32_bf16 v[120:123], v[44:47], v[184:187], v[120:123]
	v_mfma_f32_16x16x32_bf16 v[108:111], v[28:31], v[192:195], v[108:111]
	v_mfma_f32_16x16x32_bf16 v[104:107], v[44:47], v[192:195], v[104:107]
	v_mfma_f32_16x16x32_bf16 v[92:95], v[28:31], v[200:203], v[92:95]
	v_mfma_f32_16x16x32_bf16 v[88:91], v[44:47], v[200:203], v[88:91]
	s_setprio 0
	s_setprio 1
	v_mfma_f32_16x16x32_bf16 v[132:135], v[146:149], v[172:175], v[132:135]
	v_mfma_f32_16x16x32_bf16 v[128:131], v[164:167], v[172:175], v[128:131]
	v_mfma_f32_16x16x32_bf16 v[116:119], v[146:149], v[180:183], v[116:119]
	v_mfma_f32_16x16x32_bf16 v[112:115], v[164:167], v[180:183], v[112:115]
	v_mfma_f32_16x16x32_bf16 v[100:103], v[146:149], v[188:191], v[100:103]
	v_mfma_f32_16x16x32_bf16 v[96:99], v[164:167], v[188:191], v[96:99]
	v_mfma_f32_16x16x32_bf16 v[84:87], v[146:149], v[196:199], v[84:87]
	v_mfma_f32_16x16x32_bf16 v[80:83], v[164:167], v[196:199], v[80:83]
	v_mfma_f32_16x16x32_bf16 v[132:135], v[150:153], v[176:179], v[132:135]
	v_mfma_f32_16x16x32_bf16 v[128:131], v[168:171], v[176:179], v[128:131]
	v_mfma_f32_16x16x32_bf16 v[116:119], v[150:153], v[184:187], v[116:119]
	v_mfma_f32_16x16x32_bf16 v[112:115], v[168:171], v[184:187], v[112:115]
	v_mfma_f32_16x16x32_bf16 v[100:103], v[150:153], v[192:195], v[100:103]
	v_mfma_f32_16x16x32_bf16 v[96:99], v[168:171], v[192:195], v[96:99]
	v_mfma_f32_16x16x32_bf16 v[84:87], v[150:153], v[200:203], v[84:87]
	v_mfma_f32_16x16x32_bf16 v[80:83], v[168:171], v[200:203], v[80:83]
	s_setprio 0
	s_barrier
	s_mov_b32 m0, s35
	s_mov_b32 s18, s14
	s_mov_b32 s19, s15
	ds_read_b128 v[172:175], v163 offset:16384
	ds_read_b128 v[176:179], v163 offset:17408
	ds_read_b128 v[180:183], v163 offset:18432
	ds_read_b128 v[184:187], v163 offset:19456
	ds_read_b128 v[188:191], v163 offset:20480
	ds_read_b128 v[192:195], v163 offset:21504
	ds_read_b128 v[196:199], v163 offset:22528
	ds_read_b128 v[200:203], v163 offset:23552
	buffer_load_dwordx4 v154, s[16:19], s8 offen lds
	s_mov_b32 m0, s36
	s_add_i32 s9, s8, 0x80000
	buffer_load_dwordx4 v155, s[16:19], s8 offen lds
	s_mov_b32 m0, s37
	s_nop 0
	buffer_load_dwordx4 v154, s[16:19], s9 offen lds
	s_mov_b32 m0, s38
	s_nop 0
	buffer_load_dwordx4 v155, s[16:19], s9 offen lds
	s_mov_b32 m0, s34
	s_nop 0
	buffer_load_dwordx4 v156, s[12:15], s7 offen lds
	s_mov_b32 m0, s39
	s_nop 0
	buffer_load_dwordx4 v157, s[12:15], s7 offen lds
	s_waitcnt vmcnt(8)
	s_waitcnt lgkmcnt(0)
	s_barrier
	s_setprio 1
	v_mfma_f32_16x16x32_bf16 v[76:79], v[24:27], v[172:175], v[76:79]
	v_mfma_f32_16x16x32_bf16 v[72:75], v[40:43], v[172:175], v[72:75]
	v_mfma_f32_16x16x32_bf16 v[60:63], v[24:27], v[180:183], v[60:63]
	v_mfma_f32_16x16x32_bf16 v[56:59], v[40:43], v[180:183], v[56:59]
	v_mfma_f32_16x16x32_bf16 v[36:39], v[24:27], v[188:191], v[36:39]
	v_mfma_f32_16x16x32_bf16 v[32:35], v[40:43], v[188:191], v[32:35]
	v_mfma_f32_16x16x32_bf16 v[12:15], v[24:27], v[196:199], v[12:15]
	v_mfma_f32_16x16x32_bf16 v[8:11], v[40:43], v[196:199], v[8:11]
	v_mfma_f32_16x16x32_bf16 v[76:79], v[28:31], v[176:179], v[76:79]
	v_mfma_f32_16x16x32_bf16 v[72:75], v[44:47], v[176:179], v[72:75]
	v_mfma_f32_16x16x32_bf16 v[60:63], v[28:31], v[184:187], v[60:63]
	v_mfma_f32_16x16x32_bf16 v[56:59], v[44:47], v[184:187], v[56:59]
	v_mfma_f32_16x16x32_bf16 v[36:39], v[28:31], v[192:195], v[36:39]
	v_mfma_f32_16x16x32_bf16 v[32:35], v[44:47], v[192:195], v[32:35]
	v_mfma_f32_16x16x32_bf16 v[12:15], v[28:31], v[200:203], v[12:15]
	v_mfma_f32_16x16x32_bf16 v[8:11], v[44:47], v[200:203], v[8:11]
	s_setprio 0
	s_setprio 1
	v_mfma_f32_16x16x32_bf16 v[20:23], v[146:149], v[188:191], v[20:23]
	v_mfma_f32_16x16x32_bf16 v[16:19], v[164:167], v[188:191], v[16:19]
	v_mfma_f32_16x16x32_bf16 v[4:7], v[146:149], v[196:199], v[4:7]
	v_mfma_f32_16x16x32_bf16 v[0:3], v[164:167], v[196:199], v[0:3]
	v_mfma_f32_16x16x32_bf16 v[24:27], v[146:149], v[172:175], v[68:71]
	v_mfma_f32_16x16x32_bf16 v[28:31], v[164:167], v[172:175], v[64:67]
	v_mfma_f32_16x16x32_bf16 v[40:43], v[146:149], v[180:183], v[52:55]
	v_mfma_f32_16x16x32_bf16 v[44:47], v[164:167], v[180:183], v[48:51]
	v_mfma_f32_16x16x32_bf16 v[20:23], v[150:153], v[192:195], v[20:23]
	v_mfma_f32_16x16x32_bf16 v[16:19], v[168:171], v[192:195], v[16:19]
	v_mfma_f32_16x16x32_bf16 v[4:7], v[150:153], v[200:203], v[4:7]
	v_mfma_f32_16x16x32_bf16 v[0:3], v[168:171], v[200:203], v[0:3]
	v_mfma_f32_16x16x32_bf16 v[24:27], v[150:153], v[176:179], v[24:27]
	v_mfma_f32_16x16x32_bf16 v[28:31], v[168:171], v[176:179], v[28:31]
	v_mfma_f32_16x16x32_bf16 v[40:43], v[150:153], v[184:187], v[40:43]
	v_mfma_f32_16x16x32_bf16 v[44:47], v[168:171], v[184:187], v[44:47]
	s_setprio 0
	s_barrier
	v_add_u32_e32 v68, 0x18000, v162
	v_add_u32_e32 v168, 0x1c000, v162
	ds_read_b128 v[48:51], v68
	ds_read_b128 v[52:55], v68 offset:1024
	ds_read_b128 v[64:67], v68 offset:2048
	ds_read_b128 v[68:71], v68 offset:3072
	ds_read_b128 v[146:149], v168
	ds_read_b128 v[150:153], v168 offset:1024
	ds_read_b128 v[164:167], v168 offset:2048
	ds_read_b128 v[168:171], v168 offset:3072
	s_mov_b32 m0, s40
	ds_read_b128 v[172:175], v163 offset:32768
	ds_read_b128 v[176:179], v163 offset:33792
	ds_read_b128 v[180:183], v163 offset:34816
	ds_read_b128 v[184:187], v163 offset:35840
	ds_read_b128 v[188:191], v163 offset:36864
	ds_read_b128 v[192:195], v163 offset:37888
	ds_read_b128 v[196:199], v163 offset:38912
	ds_read_b128 v[200:203], v163 offset:39936
	buffer_load_dwordx4 v158, s[12:15], s7 offen lds
	s_mov_b32 m0, s41
	s_nop 0
	buffer_load_dwordx4 v159, s[12:15], s7 offen lds
	s_waitcnt vmcnt(8)
	s_waitcnt lgkmcnt(0)
	s_barrier
	s_setprio 1
	v_mfma_f32_16x16x32_bf16 v[136:139], v[48:51], v[172:175], v[136:139]
	v_mfma_f32_16x16x32_bf16 v[140:143], v[64:67], v[172:175], v[140:143]
	v_mfma_f32_16x16x32_bf16 v[124:127], v[48:51], v[180:183], v[124:127]
	v_mfma_f32_16x16x32_bf16 v[120:123], v[64:67], v[180:183], v[120:123]
	v_mfma_f32_16x16x32_bf16 v[108:111], v[48:51], v[188:191], v[108:111]
	v_mfma_f32_16x16x32_bf16 v[104:107], v[64:67], v[188:191], v[104:107]
	v_mfma_f32_16x16x32_bf16 v[92:95], v[48:51], v[196:199], v[92:95]
	v_mfma_f32_16x16x32_bf16 v[88:91], v[64:67], v[196:199], v[88:91]
	v_mfma_f32_16x16x32_bf16 v[136:139], v[52:55], v[176:179], v[136:139]
	v_mfma_f32_16x16x32_bf16 v[140:143], v[68:71], v[176:179], v[140:143]
	v_mfma_f32_16x16x32_bf16 v[124:127], v[52:55], v[184:187], v[124:127]
	v_mfma_f32_16x16x32_bf16 v[120:123], v[68:71], v[184:187], v[120:123]
	v_mfma_f32_16x16x32_bf16 v[108:111], v[52:55], v[192:195], v[108:111]
	v_mfma_f32_16x16x32_bf16 v[104:107], v[68:71], v[192:195], v[104:107]
	v_mfma_f32_16x16x32_bf16 v[92:95], v[52:55], v[200:203], v[92:95]
	v_mfma_f32_16x16x32_bf16 v[88:91], v[68:71], v[200:203], v[88:91]
	s_setprio 0
	s_setprio 1
	v_mfma_f32_16x16x32_bf16 v[132:135], v[146:149], v[172:175], v[132:135]
	v_mfma_f32_16x16x32_bf16 v[128:131], v[164:167], v[172:175], v[128:131]
	v_mfma_f32_16x16x32_bf16 v[116:119], v[146:149], v[180:183], v[116:119]
	v_mfma_f32_16x16x32_bf16 v[112:115], v[164:167], v[180:183], v[112:115]
	v_mfma_f32_16x16x32_bf16 v[100:103], v[146:149], v[188:191], v[100:103]
	v_mfma_f32_16x16x32_bf16 v[96:99], v[164:167], v[188:191], v[96:99]
	v_mfma_f32_16x16x32_bf16 v[84:87], v[146:149], v[196:199], v[84:87]
	v_mfma_f32_16x16x32_bf16 v[80:83], v[164:167], v[196:199], v[80:83]
	v_mfma_f32_16x16x32_bf16 v[132:135], v[150:153], v[176:179], v[132:135]
	v_mfma_f32_16x16x32_bf16 v[128:131], v[168:171], v[176:179], v[128:131]
	v_mfma_f32_16x16x32_bf16 v[116:119], v[150:153], v[184:187], v[116:119]
	v_mfma_f32_16x16x32_bf16 v[112:115], v[168:171], v[184:187], v[112:115]
	v_mfma_f32_16x16x32_bf16 v[100:103], v[150:153], v[192:195], v[100:103]
	v_mfma_f32_16x16x32_bf16 v[96:99], v[168:171], v[192:195], v[96:99]
	v_mfma_f32_16x16x32_bf16 v[84:87], v[150:153], v[200:203], v[84:87]
	v_mfma_f32_16x16x32_bf16 v[80:83], v[168:171], v[200:203], v[80:83]
	s_setprio 0
	s_barrier
	s_mov_b32 m0, s43
	s_or_b32 s9, s8, 0x80
	ds_read_b128 v[172:175], v163 offset:49152
	ds_read_b128 v[176:179], v163 offset:50176
	ds_read_b128 v[180:183], v163 offset:51200
	ds_read_b128 v[184:187], v163 offset:52224
	ds_read_b128 v[188:191], v163 offset:53248
	ds_read_b128 v[192:195], v163 offset:54272
	ds_read_b128 v[196:199], v163 offset:55296
	ds_read_b128 v[200:203], v163 offset:56320
	buffer_load_dwordx4 v154, s[16:19], s9 offen lds
	s_mov_b32 m0, s44
	s_add_i32 s8, s8, 0x80080
	buffer_load_dwordx4 v155, s[16:19], s9 offen lds
	s_mov_b32 m0, s47
	s_bitset1_b32 s7, 7
	buffer_load_dwordx4 v154, s[16:19], s8 offen lds
	s_mov_b32 m0, s48
	s_nop 0
	buffer_load_dwordx4 v155, s[16:19], s8 offen lds
	s_mov_b32 m0, s45
	s_nop 0
	buffer_load_dwordx4 v156, s[12:15], s7 offen lds
	s_mov_b32 m0, s46
	s_nop 0
	buffer_load_dwordx4 v157, s[12:15], s7 offen lds
	s_waitcnt vmcnt(8)
	s_waitcnt lgkmcnt(0)
	s_barrier
	s_setprio 1
	v_mfma_f32_16x16x32_bf16 v[76:79], v[48:51], v[172:175], v[76:79]
	v_mfma_f32_16x16x32_bf16 v[72:75], v[64:67], v[172:175], v[72:75]
	v_mfma_f32_16x16x32_bf16 v[60:63], v[48:51], v[180:183], v[60:63]
	v_mfma_f32_16x16x32_bf16 v[56:59], v[64:67], v[180:183], v[56:59]
	v_mfma_f32_16x16x32_bf16 v[36:39], v[48:51], v[188:191], v[36:39]
	v_mfma_f32_16x16x32_bf16 v[32:35], v[64:67], v[188:191], v[32:35]
	v_mfma_f32_16x16x32_bf16 v[12:15], v[48:51], v[196:199], v[12:15]
	v_mfma_f32_16x16x32_bf16 v[8:11], v[64:67], v[196:199], v[8:11]
	v_mfma_f32_16x16x32_bf16 v[76:79], v[52:55], v[176:179], v[76:79]
	v_mfma_f32_16x16x32_bf16 v[72:75], v[68:71], v[176:179], v[72:75]
	v_mfma_f32_16x16x32_bf16 v[60:63], v[52:55], v[184:187], v[60:63]
	v_mfma_f32_16x16x32_bf16 v[56:59], v[68:71], v[184:187], v[56:59]
	v_mfma_f32_16x16x32_bf16 v[36:39], v[52:55], v[192:195], v[36:39]
	v_mfma_f32_16x16x32_bf16 v[32:35], v[68:71], v[192:195], v[32:35]
	v_mfma_f32_16x16x32_bf16 v[12:15], v[52:55], v[200:203], v[12:15]
	v_mfma_f32_16x16x32_bf16 v[8:11], v[68:71], v[200:203], v[8:11]
	s_setprio 0
	s_setprio 1
	v_mfma_f32_16x16x32_bf16 v[24:27], v[146:149], v[172:175], v[24:27]
	v_mfma_f32_16x16x32_bf16 v[68:71], v[150:153], v[176:179], v[24:27]
	v_mfma_f32_16x16x32_bf16 v[24:27], v[164:167], v[172:175], v[28:31]
	v_mfma_f32_16x16x32_bf16 v[64:67], v[168:171], v[176:179], v[24:27]
	v_mfma_f32_16x16x32_bf16 v[24:27], v[146:149], v[180:183], v[40:43]
	v_mfma_f32_16x16x32_bf16 v[52:55], v[150:153], v[184:187], v[24:27]
	v_mfma_f32_16x16x32_bf16 v[24:27], v[164:167], v[180:183], v[44:47]
	v_mfma_f32_16x16x32_bf16 v[20:23], v[146:149], v[188:191], v[20:23]
	v_mfma_f32_16x16x32_bf16 v[16:19], v[164:167], v[188:191], v[16:19]
	v_mfma_f32_16x16x32_bf16 v[4:7], v[146:149], v[196:199], v[4:7]
	v_mfma_f32_16x16x32_bf16 v[0:3], v[164:167], v[196:199], v[0:3]
	v_mfma_f32_16x16x32_bf16 v[48:51], v[168:171], v[184:187], v[24:27]
	v_mfma_f32_16x16x32_bf16 v[20:23], v[150:153], v[192:195], v[20:23]
	v_mfma_f32_16x16x32_bf16 v[16:19], v[168:171], v[192:195], v[16:19]
	v_mfma_f32_16x16x32_bf16 v[4:7], v[150:153], v[200:203], v[4:7]
	v_mfma_f32_16x16x32_bf16 v[0:3], v[168:171], v[200:203], v[0:3]
	s_setprio 0
	s_barrier
	s_add_i32 s6, s6, 2
	s_addk_i32 s4, 0x100
	s_addk_i32 s5, 0x100
	s_cmp_gt_u32 s6, 29
	s_cbranch_scc0 .LBB0_326
	s_and_b64 vcc, exec, s[24:25]
	s_cbranch_vccz .LBB0_329
	s_barrier

.LBB0_871:
	s_add_i32 s51, s51, 2
	s_cmp_lt_u32 s51, 14
	s_cselect_b32 s15, 0, 0x1fff800
	s_cselect_b32 s53, 0, 0x3ff800
	s_add_i32 s15, s49, s15
	s_add_i32 s52, s14, 0x100
	s_add_i32 s53, s50, s53
	v_add_u32_e32 v140, 0x10000, v202
	v_add_u32_e32 v216, 0x14000, v202
	s_add_i32 s15, s52, s15
	s_add_i32 s54, s53, s14
	ds_read_b128 v[128:131], v140
	ds_read_b128 v[132:135], v140 offset:1024
	ds_read_b128 v[136:139], v140 offset:2048
	ds_read_b128 v[140:143], v140 offset:3072
	ds_read_b128 v[204:207], v216
	ds_read_b128 v[208:211], v216 offset:1024
	ds_read_b128 v[212:215], v216 offset:2048
	ds_read_b128 v[216:219], v216 offset:3072
	s_cmp_lt_u32 s51, 16
	s_cselect_b32 s53, 0, 0x1fff800
	s_add_i32 s53, s49, s53
	s_add_i32 s53, s53, s14
	s_add_i32 s55, s53, 0x80
	s_cmpk_eq_i32 s14, 0xf00
	s_cselect_b32 s53, s47, s15
	s_mov_b32 m0, s42
	ds_read_b128 v[220:223], v203
	ds_read_b128 v[224:227], v203 offset:1024
	ds_read_b128 v[228:231], v203 offset:2048
	ds_read_b128 v[232:235], v203 offset:3072
	ds_read_b128 v[236:239], v203 offset:4096
	ds_read_b128 v[240:243], v203 offset:5120
	ds_read_b128 v[244:247], v203 offset:6144
	ds_read_b128 v[248:251], v203 offset:7168
	buffer_load_dwordx4 v198, s[8:11], s55 offen lds
	s_mov_b32 m0, s43
	s_cselect_b32 s54, s48, s54
	buffer_load_dwordx4 v199, s[8:11], s55 offen lds
	s_waitcnt vmcnt(8)
	s_waitcnt lgkmcnt(0)
	s_barrier
	s_setprio 1
	v_mfma_f32_16x16x32_bf16 v[124:127], v[128:131], v[220:223], v[124:127]
	v_mfma_f32_16x16x32_bf16 v[120:123], v[136:139], v[220:223], v[120:123]
	v_mfma_f32_16x16x32_bf16 v[108:111], v[128:131], v[228:231], v[108:111]
	v_mfma_f32_16x16x32_bf16 v[104:107], v[136:139], v[228:231], v[104:107]
	v_mfma_f32_16x16x32_bf16 v[92:95], v[128:131], v[236:239], v[92:95]
	v_mfma_f32_16x16x32_bf16 v[88:91], v[136:139], v[236:239], v[88:91]
	v_mfma_f32_16x16x32_bf16 v[76:79], v[128:131], v[244:247], v[76:79]
	v_mfma_f32_16x16x32_bf16 v[72:75], v[136:139], v[244:247], v[72:75]
	v_mfma_f32_16x16x32_bf16 v[124:127], v[132:135], v[224:227], v[124:127]
	v_mfma_f32_16x16x32_bf16 v[120:123], v[140:143], v[224:227], v[120:123]
	v_mfma_f32_16x16x32_bf16 v[108:111], v[132:135], v[232:235], v[108:111]
	v_mfma_f32_16x16x32_bf16 v[104:107], v[140:143], v[232:235], v[104:107]
	v_mfma_f32_16x16x32_bf16 v[92:95], v[132:135], v[240:243], v[92:95]
	v_mfma_f32_16x16x32_bf16 v[88:91], v[140:143], v[240:243], v[88:91]
	v_mfma_f32_16x16x32_bf16 v[76:79], v[132:135], v[248:251], v[76:79]
	v_mfma_f32_16x16x32_bf16 v[72:75], v[140:143], v[248:251], v[72:75]
	s_setprio 0
	s_setprio 1
	v_mfma_f32_16x16x32_bf16 v[116:119], v[204:207], v[220:223], v[116:119]
	v_mfma_f32_16x16x32_bf16 v[112:115], v[212:215], v[220:223], v[112:115]
	v_mfma_f32_16x16x32_bf16 v[100:103], v[204:207], v[228:231], v[100:103]
	v_mfma_f32_16x16x32_bf16 v[96:99], v[212:215], v[228:231], v[96:99]
	v_mfma_f32_16x16x32_bf16 v[84:87], v[204:207], v[236:239], v[84:87]
	v_mfma_f32_16x16x32_bf16 v[80:83], v[212:215], v[236:239], v[80:83]
	v_mfma_f32_16x16x32_bf16 v[68:71], v[204:207], v[244:247], v[68:71]
	v_mfma_f32_16x16x32_bf16 v[64:67], v[212:215], v[244:247], v[64:67]
	v_mfma_f32_16x16x32_bf16 v[116:119], v[208:211], v[224:227], v[116:119]
	v_mfma_f32_16x16x32_bf16 v[112:115], v[216:219], v[224:227], v[112:115]
	v_mfma_f32_16x16x32_bf16 v[100:103], v[208:211], v[232:235], v[100:103]
	v_mfma_f32_16x16x32_bf16 v[96:99], v[216:219], v[232:235], v[96:99]
	v_mfma_f32_16x16x32_bf16 v[84:87], v[208:211], v[240:243], v[84:87]
	v_mfma_f32_16x16x32_bf16 v[80:83], v[216:219], v[240:243], v[80:83]
	v_mfma_f32_16x16x32_bf16 v[68:71], v[208:211], v[248:251], v[68:71]
	v_mfma_f32_16x16x32_bf16 v[64:67], v[216:219], v[248:251], v[64:67]
	s_setprio 0
	s_barrier
	s_mov_b32 m0, s27
	s_mov_b32 s14, s10
	s_mov_b32 s15, s11
	ds_read_b128 v[220:223], v203 offset:16384
	ds_read_b128 v[224:227], v203 offset:17408
	ds_read_b128 v[228:231], v203 offset:18432
	ds_read_b128 v[232:235], v203 offset:19456
	ds_read_b128 v[236:239], v203 offset:20480
	ds_read_b128 v[240:243], v203 offset:21504
	ds_read_b128 v[244:247], v203 offset:22528
	ds_read_b128 v[248:251], v203 offset:23552
	buffer_load_dwordx4 v194, s[12:15], s54 offen lds
	s_mov_b32 m0, s28
	s_add_i32 s55, s54, 0x40000
	buffer_load_dwordx4 v195, s[12:15], s54 offen lds
	s_mov_b32 m0, s29
	s_nop 0
	buffer_load_dwordx4 v194, s[12:15], s55 offen lds
	s_mov_b32 m0, s30
	s_nop 0
	buffer_load_dwordx4 v195, s[12:15], s55 offen lds
	s_mov_b32 m0, s26
	s_nop 0
	buffer_load_dwordx4 v196, s[8:11], s53 offen lds
	s_mov_b32 m0, s31
	s_nop 0
	buffer_load_dwordx4 v197, s[8:11], s53 offen lds
	s_waitcnt vmcnt(8)
	s_waitcnt lgkmcnt(0)
	s_barrier
	s_setprio 1
	v_mfma_f32_16x16x32_bf16 v[60:63], v[128:131], v[220:223], v[60:63]
	v_mfma_f32_16x16x32_bf16 v[56:59], v[136:139], v[220:223], v[56:59]
	v_mfma_f32_16x16x32_bf16 v[44:47], v[128:131], v[228:231], v[44:47]
	v_mfma_f32_16x16x32_bf16 v[40:43], v[136:139], v[228:231], v[40:43]
	v_mfma_f32_16x16x32_bf16 v[28:31], v[128:131], v[236:239], v[28:31]
	v_mfma_f32_16x16x32_bf16 v[24:27], v[136:139], v[236:239], v[24:27]
	v_mfma_f32_16x16x32_bf16 v[12:15], v[128:131], v[244:247], v[12:15]
	v_mfma_f32_16x16x32_bf16 v[8:11], v[136:139], v[244:247], v[8:11]
	v_mfma_f32_16x16x32_bf16 v[60:63], v[132:135], v[224:227], v[60:63]
	v_mfma_f32_16x16x32_bf16 v[56:59], v[140:143], v[224:227], v[56:59]
	v_mfma_f32_16x16x32_bf16 v[44:47], v[132:135], v[232:235], v[44:47]
	v_mfma_f32_16x16x32_bf16 v[40:43], v[140:143], v[232:235], v[40:43]
	v_mfma_f32_16x16x32_bf16 v[28:31], v[132:135], v[240:243], v[28:31]
	v_mfma_f32_16x16x32_bf16 v[24:27], v[140:143], v[240:243], v[24:27]
	v_mfma_f32_16x16x32_bf16 v[12:15], v[132:135], v[248:251], v[12:15]
	v_mfma_f32_16x16x32_bf16 v[8:11], v[140:143], v[248:251], v[8:11]
	s_setprio 0
	s_setprio 1
	v_mfma_f32_16x16x32_bf16 v[52:55], v[204:207], v[220:223], v[52:55]
	v_mfma_f32_16x16x32_bf16 v[48:51], v[212:215], v[220:223], v[48:51]
	v_mfma_f32_16x16x32_bf16 v[36:39], v[204:207], v[228:231], v[36:39]
	v_mfma_f32_16x16x32_bf16 v[32:35], v[212:215], v[228:231], v[32:35]
	v_mfma_f32_16x16x32_bf16 v[20:23], v[204:207], v[236:239], v[20:23]
	v_mfma_f32_16x16x32_bf16 v[16:19], v[212:215], v[236:239], v[16:19]
	v_mfma_f32_16x16x32_bf16 v[0:3], v[204:207], v[244:247], v[0:3]
	v_mfma_f32_16x16x32_bf16 v[4:7], v[212:215], v[244:247], v[4:7]
	v_mfma_f32_16x16x32_bf16 v[52:55], v[208:211], v[224:227], v[52:55]
	v_mfma_f32_16x16x32_bf16 v[48:51], v[216:219], v[224:227], v[48:51]
	v_mfma_f32_16x16x32_bf16 v[36:39], v[208:211], v[232:235], v[36:39]
	v_mfma_f32_16x16x32_bf16 v[32:35], v[216:219], v[232:235], v[32:35]
	v_mfma_f32_16x16x32_bf16 v[20:23], v[208:211], v[240:243], v[20:23]
	v_mfma_f32_16x16x32_bf16 v[16:19], v[216:219], v[240:243], v[16:19]
	v_mfma_f32_16x16x32_bf16 v[0:3], v[208:211], v[248:251], v[0:3]
	v_mfma_f32_16x16x32_bf16 v[4:7], v[216:219], v[248:251], v[4:7]
	s_setprio 0
	s_barrier
	v_add_u32_e32 v140, 0x18000, v202
	v_add_u32_e32 v216, 0x1c000, v202
	ds_read_b128 v[128:131], v140
	ds_read_b128 v[132:135], v140 offset:1024
	ds_read_b128 v[136:139], v140 offset:2048
	ds_read_b128 v[140:143], v140 offset:3072
	ds_read_b128 v[204:207], v216
	ds_read_b128 v[208:211], v216 offset:1024
	ds_read_b128 v[212:215], v216 offset:2048
	ds_read_b128 v[216:219], v216 offset:3072
	s_mov_b32 m0, s33
	ds_read_b128 v[220:223], v203 offset:32768
	ds_read_b128 v[224:227], v203 offset:33792
	ds_read_b128 v[228:231], v203 offset:34816
	ds_read_b128 v[232:235], v203 offset:35840
	ds_read_b128 v[236:239], v203 offset:36864
	ds_read_b128 v[240:243], v203 offset:37888
	ds_read_b128 v[244:247], v203 offset:38912
	ds_read_b128 v[248:251], v203 offset:39936
	buffer_load_dwordx4 v198, s[8:11], s53 offen lds
	s_mov_b32 m0, s34
	s_nop 0
	buffer_load_dwordx4 v199, s[8:11], s53 offen lds
	s_waitcnt vmcnt(8)
	s_waitcnt lgkmcnt(0)
	s_barrier
	s_setprio 1
	v_mfma_f32_16x16x32_bf16 v[124:127], v[128:131], v[220:223], v[124:127]
	v_mfma_f32_16x16x32_bf16 v[120:123], v[136:139], v[220:223], v[120:123]
	v_mfma_f32_16x16x32_bf16 v[108:111], v[128:131], v[228:231], v[108:111]
	v_mfma_f32_16x16x32_bf16 v[104:107], v[136:139], v[228:231], v[104:107]
	v_mfma_f32_16x16x32_bf16 v[92:95], v[128:131], v[236:239], v[92:95]
	v_mfma_f32_16x16x32_bf16 v[88:91], v[136:139], v[236:239], v[88:91]
	v_mfma_f32_16x16x32_bf16 v[76:79], v[128:131], v[244:247], v[76:79]
	v_mfma_f32_16x16x32_bf16 v[72:75], v[136:139], v[244:247], v[72:75]
	v_mfma_f32_16x16x32_bf16 v[124:127], v[132:135], v[224:227], v[124:127]
	v_mfma_f32_16x16x32_bf16 v[120:123], v[140:143], v[224:227], v[120:123]
	v_mfma_f32_16x16x32_bf16 v[108:111], v[132:135], v[232:235], v[108:111]
	v_mfma_f32_16x16x32_bf16 v[104:107], v[140:143], v[232:235], v[104:107]
	v_mfma_f32_16x16x32_bf16 v[92:95], v[132:135], v[240:243], v[92:95]
	v_mfma_f32_16x16x32_bf16 v[88:91], v[140:143], v[240:243], v[88:91]
	v_mfma_f32_16x16x32_bf16 v[76:79], v[132:135], v[248:251], v[76:79]
	v_mfma_f32_16x16x32_bf16 v[72:75], v[140:143], v[248:251], v[72:75]
	s_setprio 0
	s_setprio 1
	v_mfma_f32_16x16x32_bf16 v[116:119], v[204:207], v[220:223], v[116:119]
	v_mfma_f32_16x16x32_bf16 v[112:115], v[212:215], v[220:223], v[112:115]
	v_mfma_f32_16x16x32_bf16 v[100:103], v[204:207], v[228:231], v[100:103]
	v_mfma_f32_16x16x32_bf16 v[96:99], v[212:215], v[228:231], v[96:99]
	v_mfma_f32_16x16x32_bf16 v[84:87], v[204:207], v[236:239], v[84:87]
	v_mfma_f32_16x16x32_bf16 v[80:83], v[212:215], v[236:239], v[80:83]
	v_mfma_f32_16x16x32_bf16 v[68:71], v[204:207], v[244:247], v[68:71]
	v_mfma_f32_16x16x32_bf16 v[64:67], v[212:215], v[244:247], v[64:67]
	v_mfma_f32_16x16x32_bf16 v[116:119], v[208:211], v[224:227], v[116:119]
	v_mfma_f32_16x16x32_bf16 v[112:115], v[216:219], v[224:227], v[112:115]
	v_mfma_f32_16x16x32_bf16 v[100:103], v[208:211], v[232:235], v[100:103]
	v_mfma_f32_16x16x32_bf16 v[96:99], v[216:219], v[232:235], v[96:99]
	v_mfma_f32_16x16x32_bf16 v[84:87], v[208:211], v[240:243], v[84:87]
	v_mfma_f32_16x16x32_bf16 v[80:83], v[216:219], v[240:243], v[80:83]
	v_mfma_f32_16x16x32_bf16 v[68:71], v[208:211], v[248:251], v[68:71]
	v_mfma_f32_16x16x32_bf16 v[64:67], v[216:219], v[248:251], v[64:67]
	s_setprio 0
	s_barrier
	s_mov_b32 m0, s36
	s_or_b32 s55, s54, 0x80
	ds_read_b128 v[220:223], v203 offset:49152
	ds_read_b128 v[224:227], v203 offset:50176
	ds_read_b128 v[228:231], v203 offset:51200
	ds_read_b128 v[232:235], v203 offset:52224
	ds_read_b128 v[236:239], v203 offset:53248
	ds_read_b128 v[240:243], v203 offset:54272
	ds_read_b128 v[244:247], v203 offset:55296
	ds_read_b128 v[248:251], v203 offset:56320
	buffer_load_dwordx4 v194, s[12:15], s55 offen lds
	s_mov_b32 m0, s37
	s_add_i32 s54, s54, 0x40080
	buffer_load_dwordx4 v195, s[12:15], s55 offen lds
	s_mov_b32 m0, s40
	s_bitset1_b32 s53, 7
	buffer_load_dwordx4 v194, s[12:15], s54 offen lds
	s_mov_b32 m0, s41
	s_nop 0
	buffer_load_dwordx4 v195, s[12:15], s54 offen lds
	s_mov_b32 m0, s38
	s_nop 0
	buffer_load_dwordx4 v196, s[8:11], s53 offen lds
	s_mov_b32 m0, s39
	s_nop 0
	buffer_load_dwordx4 v197, s[8:11], s53 offen lds
	s_waitcnt vmcnt(8)
	s_waitcnt lgkmcnt(0)
	s_barrier
	s_setprio 1
	v_mfma_f32_16x16x32_bf16 v[60:63], v[128:131], v[220:223], v[60:63]
	v_mfma_f32_16x16x32_bf16 v[56:59], v[136:139], v[220:223], v[56:59]
	v_mfma_f32_16x16x32_bf16 v[44:47], v[128:131], v[228:231], v[44:47]
	v_mfma_f32_16x16x32_bf16 v[40:43], v[136:139], v[228:231], v[40:43]
	v_mfma_f32_16x16x32_bf16 v[28:31], v[128:131], v[236:239], v[28:31]
	v_mfma_f32_16x16x32_bf16 v[24:27], v[136:139], v[236:239], v[24:27]
	v_mfma_f32_16x16x32_bf16 v[12:15], v[128:131], v[244:247], v[12:15]
	v_mfma_f32_16x16x32_bf16 v[8:11], v[136:139], v[244:247], v[8:11]
	v_mfma_f32_16x16x32_bf16 v[60:63], v[132:135], v[224:227], v[60:63]
	v_mfma_f32_16x16x32_bf16 v[56:59], v[140:143], v[224:227], v[56:59]
	v_mfma_f32_16x16x32_bf16 v[44:47], v[132:135], v[232:235], v[44:47]
	v_mfma_f32_16x16x32_bf16 v[40:43], v[140:143], v[232:235], v[40:43]
	v_mfma_f32_16x16x32_bf16 v[28:31], v[132:135], v[240:243], v[28:31]
	v_mfma_f32_16x16x32_bf16 v[24:27], v[140:143], v[240:243], v[24:27]
	v_mfma_f32_16x16x32_bf16 v[12:15], v[132:135], v[248:251], v[12:15]
	v_mfma_f32_16x16x32_bf16 v[8:11], v[140:143], v[248:251], v[8:11]
	s_setprio 0
	s_setprio 1
	v_mfma_f32_16x16x32_bf16 v[52:55], v[204:207], v[220:223], v[52:55]
	v_mfma_f32_16x16x32_bf16 v[48:51], v[212:215], v[220:223], v[48:51]
	v_mfma_f32_16x16x32_bf16 v[36:39], v[204:207], v[228:231], v[36:39]
	v_mfma_f32_16x16x32_bf16 v[32:35], v[212:215], v[228:231], v[32:35]
	v_mfma_f32_16x16x32_bf16 v[20:23], v[204:207], v[236:239], v[20:23]
	v_mfma_f32_16x16x32_bf16 v[16:19], v[212:215], v[236:239], v[16:19]
	v_mfma_f32_16x16x32_bf16 v[0:3], v[204:207], v[244:247], v[0:3]
	v_mfma_f32_16x16x32_bf16 v[4:7], v[212:215], v[244:247], v[4:7]
	v_mfma_f32_16x16x32_bf16 v[52:55], v[208:211], v[224:227], v[52:55]
	v_mfma_f32_16x16x32_bf16 v[48:51], v[216:219], v[224:227], v[48:51]
	v_mfma_f32_16x16x32_bf16 v[36:39], v[208:211], v[232:235], v[36:39]
	v_mfma_f32_16x16x32_bf16 v[32:35], v[216:219], v[232:235], v[32:35]
	v_mfma_f32_16x16x32_bf16 v[20:23], v[208:211], v[240:243], v[20:23]
	v_mfma_f32_16x16x32_bf16 v[16:19], v[216:219], v[240:243], v[16:19]
	v_mfma_f32_16x16x32_bf16 v[0:3], v[208:211], v[248:251], v[0:3]
	v_mfma_f32_16x16x32_bf16 v[4:7], v[216:219], v[248:251], v[4:7]
	s_setprio 0
	s_barrier
	s_cmp_gt_u32 s51, 29
	s_cbranch_scc1 .LBB0_873
	s_mov_b32 s14, s52
	s_cmpk_lg_i32 s14, 0x800
	s_cbranch_scc0 .LBB0_870
	s_branch .LBB0_871

.LBB0_955:
	v_add_u32_e32 v150, 0x10000, v136
	v_add_u32_e32 v166, 0x14000, v136
	ds_read_b128 v[138:141], v150
	ds_read_b128 v[142:145], v150 offset:1024
	ds_read_b128 v[146:149], v150 offset:2048
	ds_read_b128 v[150:153], v150 offset:3072
	ds_read_b128 v[154:157], v166
	ds_read_b128 v[158:161], v166 offset:1024
	ds_read_b128 v[162:165], v166 offset:2048
	ds_read_b128 v[166:169], v166 offset:3072
	s_cmp_eq_u32 s56, 28
	s_cselect_b32 s57, s50, s54
	s_cselect_b32 s58, s51, s55
	s_add_i32 s10, s54, 0xffffff80
	s_mov_b32 m0, s43
	ds_read_b128 v[170:173], v137
	ds_read_b128 v[174:177], v137 offset:1024
	ds_read_b128 v[178:181], v137 offset:2048
	ds_read_b128 v[182:185], v137 offset:3072
	ds_read_b128 v[186:189], v137 offset:4096
	ds_read_b128 v[190:193], v137 offset:5120
	ds_read_b128 v[194:197], v137 offset:6144
	ds_read_b128 v[198:201], v137 offset:7168
	buffer_load_dwordx4 v132, s[4:7], s10 offen lds
	s_mov_b32 m0, s44
	s_nop 0
	buffer_load_dwordx4 v133, s[4:7], s10 offen lds
	s_waitcnt vmcnt(8)
	s_waitcnt lgkmcnt(0)
	s_barrier
	s_setprio 1
	v_mfma_f32_16x16x32_bf16 v[120:123], v[138:141], v[170:173], v[120:123]
	v_mfma_f32_16x16x32_bf16 v[112:115], v[146:149], v[170:173], v[112:115]
	v_mfma_f32_16x16x32_bf16 v[100:103], v[138:141], v[178:181], v[100:103]
	v_mfma_f32_16x16x32_bf16 v[96:99], v[146:149], v[178:181], v[96:99]
	v_mfma_f32_16x16x32_bf16 v[84:87], v[138:141], v[186:189], v[84:87]
	v_mfma_f32_16x16x32_bf16 v[80:83], v[146:149], v[186:189], v[80:83]
	v_mfma_f32_16x16x32_bf16 v[68:71], v[138:141], v[194:197], v[68:71]
	v_mfma_f32_16x16x32_bf16 v[64:67], v[146:149], v[194:197], v[64:67]
	v_mfma_f32_16x16x32_bf16 v[120:123], v[142:145], v[174:177], v[120:123]
	v_mfma_f32_16x16x32_bf16 v[112:115], v[150:153], v[174:177], v[112:115]
	v_mfma_f32_16x16x32_bf16 v[100:103], v[142:145], v[182:185], v[100:103]
	v_mfma_f32_16x16x32_bf16 v[96:99], v[150:153], v[182:185], v[96:99]
	v_mfma_f32_16x16x32_bf16 v[84:87], v[142:145], v[190:193], v[84:87]
	v_mfma_f32_16x16x32_bf16 v[80:83], v[150:153], v[190:193], v[80:83]
	v_mfma_f32_16x16x32_bf16 v[68:71], v[142:145], v[198:201], v[68:71]
	v_mfma_f32_16x16x32_bf16 v[64:67], v[150:153], v[198:201], v[64:67]
	s_setprio 0
	s_setprio 1
	v_mfma_f32_16x16x32_bf16 v[124:127], v[154:157], v[170:173], v[124:127]
	v_mfma_f32_16x16x32_bf16 v[116:119], v[162:165], v[170:173], v[116:119]
	v_mfma_f32_16x16x32_bf16 v[108:111], v[154:157], v[178:181], v[108:111]
	v_mfma_f32_16x16x32_bf16 v[104:107], v[162:165], v[178:181], v[104:107]
	v_mfma_f32_16x16x32_bf16 v[92:95], v[154:157], v[186:189], v[92:95]
	v_mfma_f32_16x16x32_bf16 v[88:91], v[162:165], v[186:189], v[88:91]
	v_mfma_f32_16x16x32_bf16 v[76:79], v[154:157], v[194:197], v[76:79]
	v_mfma_f32_16x16x32_bf16 v[72:75], v[162:165], v[194:197], v[72:75]
	v_mfma_f32_16x16x32_bf16 v[124:127], v[158:161], v[174:177], v[124:127]
	v_mfma_f32_16x16x32_bf16 v[116:119], v[166:169], v[174:177], v[116:119]
	v_mfma_f32_16x16x32_bf16 v[108:111], v[158:161], v[182:185], v[108:111]
	v_mfma_f32_16x16x32_bf16 v[104:107], v[166:169], v[182:185], v[104:107]
	v_mfma_f32_16x16x32_bf16 v[92:95], v[158:161], v[190:193], v[92:95]
	v_mfma_f32_16x16x32_bf16 v[88:91], v[166:169], v[190:193], v[88:91]
	v_mfma_f32_16x16x32_bf16 v[76:79], v[158:161], v[198:201], v[76:79]
	v_mfma_f32_16x16x32_bf16 v[72:75], v[166:169], v[198:201], v[72:75]
	s_setprio 0
	s_barrier
	s_mov_b32 m0, s27
	s_mov_b32 s10, s6
	s_mov_b32 s11, s7
	ds_read_b128 v[170:173], v137 offset:16384
	ds_read_b128 v[174:177], v137 offset:17408
	ds_read_b128 v[178:181], v137 offset:18432
	ds_read_b128 v[182:185], v137 offset:19456
	ds_read_b128 v[186:189], v137 offset:20480
	ds_read_b128 v[190:193], v137 offset:21504
	ds_read_b128 v[194:197], v137 offset:22528
	ds_read_b128 v[198:201], v137 offset:23552
	buffer_load_dwordx4 v128, s[8:11], s58 offen lds
	s_mov_b32 m0, s28
	s_add_i32 s59, s58, 0x80000
	buffer_load_dwordx4 v129, s[8:11], s58 offen lds
	s_mov_b32 m0, s29
	s_nop 0
	buffer_load_dwordx4 v128, s[8:11], s59 offen lds
	s_mov_b32 m0, s30
	s_nop 0
	buffer_load_dwordx4 v129, s[8:11], s59 offen lds
	s_mov_b32 m0, s26
	s_nop 0
	buffer_load_dwordx4 v130, s[4:7], s57 offen lds
	s_mov_b32 m0, s31
	s_nop 0
	buffer_load_dwordx4 v131, s[4:7], s57 offen lds
	s_waitcnt vmcnt(8)
	s_waitcnt lgkmcnt(0)
	s_barrier
	s_setprio 1
	v_mfma_f32_16x16x32_bf16 v[56:59], v[138:141], v[170:173], v[56:59]
	v_mfma_f32_16x16x32_bf16 v[48:51], v[146:149], v[170:173], v[48:51]
	v_mfma_f32_16x16x32_bf16 v[40:43], v[138:141], v[178:181], v[40:43]
	v_mfma_f32_16x16x32_bf16 v[32:35], v[146:149], v[178:181], v[32:35]
	v_mfma_f32_16x16x32_bf16 v[24:27], v[138:141], v[186:189], v[24:27]
	v_mfma_f32_16x16x32_bf16 v[16:19], v[146:149], v[186:189], v[16:19]
	v_mfma_f32_16x16x32_bf16 v[4:7], v[138:141], v[194:197], v[4:7]
	v_mfma_f32_16x16x32_bf16 v[0:3], v[146:149], v[194:197], v[0:3]
	v_mfma_f32_16x16x32_bf16 v[56:59], v[142:145], v[174:177], v[56:59]
	v_mfma_f32_16x16x32_bf16 v[48:51], v[150:153], v[174:177], v[48:51]
	v_mfma_f32_16x16x32_bf16 v[40:43], v[142:145], v[182:185], v[40:43]
	v_mfma_f32_16x16x32_bf16 v[32:35], v[150:153], v[182:185], v[32:35]
	v_mfma_f32_16x16x32_bf16 v[24:27], v[142:145], v[190:193], v[24:27]
	v_mfma_f32_16x16x32_bf16 v[16:19], v[150:153], v[190:193], v[16:19]
	v_mfma_f32_16x16x32_bf16 v[4:7], v[142:145], v[198:201], v[4:7]
	v_mfma_f32_16x16x32_bf16 v[0:3], v[150:153], v[198:201], v[0:3]
	s_setprio 0
	s_setprio 1
	v_mfma_f32_16x16x32_bf16 v[60:63], v[154:157], v[170:173], v[60:63]
	v_mfma_f32_16x16x32_bf16 v[52:55], v[162:165], v[170:173], v[52:55]
	v_mfma_f32_16x16x32_bf16 v[44:47], v[154:157], v[178:181], v[44:47]
	v_mfma_f32_16x16x32_bf16 v[36:39], v[162:165], v[178:181], v[36:39]
	v_mfma_f32_16x16x32_bf16 v[28:31], v[154:157], v[186:189], v[28:31]
	v_mfma_f32_16x16x32_bf16 v[20:23], v[162:165], v[186:189], v[20:23]
	v_mfma_f32_16x16x32_bf16 v[8:11], v[154:157], v[194:197], v[8:11]
	v_mfma_f32_16x16x32_bf16 v[12:15], v[162:165], v[194:197], v[12:15]
	v_mfma_f32_16x16x32_bf16 v[60:63], v[158:161], v[174:177], v[60:63]
	v_mfma_f32_16x16x32_bf16 v[52:55], v[166:169], v[174:177], v[52:55]
	v_mfma_f32_16x16x32_bf16 v[44:47], v[158:161], v[182:185], v[44:47]
	v_mfma_f32_16x16x32_bf16 v[36:39], v[166:169], v[182:185], v[36:39]
	v_mfma_f32_16x16x32_bf16 v[28:31], v[158:161], v[190:193], v[28:31]
	v_mfma_f32_16x16x32_bf16 v[20:23], v[166:169], v[190:193], v[20:23]
	v_mfma_f32_16x16x32_bf16 v[8:11], v[158:161], v[198:201], v[8:11]
	v_mfma_f32_16x16x32_bf16 v[12:15], v[166:169], v[198:201], v[12:15]
	s_setprio 0
	s_barrier
	v_add_u32_e32 v150, 0x18000, v136
	v_add_u32_e32 v166, 0x1c000, v136
	ds_read_b128 v[138:141], v150
	ds_read_b128 v[142:145], v150 offset:1024
	ds_read_b128 v[146:149], v150 offset:2048
	ds_read_b128 v[150:153], v150 offset:3072
	ds_read_b128 v[154:157], v166
	ds_read_b128 v[158:161], v166 offset:1024
	ds_read_b128 v[162:165], v166 offset:2048
	ds_read_b128 v[166:169], v166 offset:3072
	s_mov_b32 m0, s33
	ds_read_b128 v[170:173], v137 offset:32768
	ds_read_b128 v[174:177], v137 offset:33792
	ds_read_b128 v[178:181], v137 offset:34816
	ds_read_b128 v[182:185], v137 offset:35840
	ds_read_b128 v[186:189], v137 offset:36864
	ds_read_b128 v[190:193], v137 offset:37888
	ds_read_b128 v[194:197], v137 offset:38912
	ds_read_b128 v[198:201], v137 offset:39936
	buffer_load_dwordx4 v132, s[4:7], s57 offen lds
	s_mov_b32 m0, s34
	s_nop 0
	buffer_load_dwordx4 v133, s[4:7], s57 offen lds
	s_waitcnt vmcnt(8)
	s_waitcnt lgkmcnt(0)
	s_barrier
	s_setprio 1
	v_mfma_f32_16x16x32_bf16 v[120:123], v[138:141], v[170:173], v[120:123]
	v_mfma_f32_16x16x32_bf16 v[112:115], v[146:149], v[170:173], v[112:115]
	v_mfma_f32_16x16x32_bf16 v[100:103], v[138:141], v[178:181], v[100:103]
	v_mfma_f32_16x16x32_bf16 v[96:99], v[146:149], v[178:181], v[96:99]
	v_mfma_f32_16x16x32_bf16 v[84:87], v[138:141], v[186:189], v[84:87]
	v_mfma_f32_16x16x32_bf16 v[80:83], v[146:149], v[186:189], v[80:83]
	v_mfma_f32_16x16x32_bf16 v[68:71], v[138:141], v[194:197], v[68:71]
	v_mfma_f32_16x16x32_bf16 v[64:67], v[146:149], v[194:197], v[64:67]
	v_mfma_f32_16x16x32_bf16 v[120:123], v[142:145], v[174:177], v[120:123]
	v_mfma_f32_16x16x32_bf16 v[112:115], v[150:153], v[174:177], v[112:115]
	v_mfma_f32_16x16x32_bf16 v[100:103], v[142:145], v[182:185], v[100:103]
	v_mfma_f32_16x16x32_bf16 v[96:99], v[150:153], v[182:185], v[96:99]
	v_mfma_f32_16x16x32_bf16 v[84:87], v[142:145], v[190:193], v[84:87]
	v_mfma_f32_16x16x32_bf16 v[80:83], v[150:153], v[190:193], v[80:83]
	v_mfma_f32_16x16x32_bf16 v[68:71], v[142:145], v[198:201], v[68:71]
	v_mfma_f32_16x16x32_bf16 v[64:67], v[150:153], v[198:201], v[64:67]
	s_setprio 0
	s_setprio 1
	v_mfma_f32_16x16x32_bf16 v[124:127], v[154:157], v[170:173], v[124:127]
	v_mfma_f32_16x16x32_bf16 v[116:119], v[162:165], v[170:173], v[116:119]
	v_mfma_f32_16x16x32_bf16 v[108:111], v[154:157], v[178:181], v[108:111]
	v_mfma_f32_16x16x32_bf16 v[104:107], v[162:165], v[178:181], v[104:107]
	v_mfma_f32_16x16x32_bf16 v[92:95], v[154:157], v[186:189], v[92:95]
	v_mfma_f32_16x16x32_bf16 v[88:91], v[162:165], v[186:189], v[88:91]
	v_mfma_f32_16x16x32_bf16 v[76:79], v[154:157], v[194:197], v[76:79]
	v_mfma_f32_16x16x32_bf16 v[72:75], v[162:165], v[194:197], v[72:75]
	v_mfma_f32_16x16x32_bf16 v[124:127], v[158:161], v[174:177], v[124:127]
	v_mfma_f32_16x16x32_bf16 v[116:119], v[166:169], v[174:177], v[116:119]
	v_mfma_f32_16x16x32_bf16 v[108:111], v[158:161], v[182:185], v[108:111]
	v_mfma_f32_16x16x32_bf16 v[104:107], v[166:169], v[182:185], v[104:107]
	v_mfma_f32_16x16x32_bf16 v[92:95], v[158:161], v[190:193], v[92:95]
	v_mfma_f32_16x16x32_bf16 v[88:91], v[166:169], v[190:193], v[88:91]
	v_mfma_f32_16x16x32_bf16 v[76:79], v[158:161], v[198:201], v[76:79]
	v_mfma_f32_16x16x32_bf16 v[72:75], v[166:169], v[198:201], v[72:75]
	s_setprio 0
	s_barrier
	s_mov_b32 m0, s37
	s_or_b32 s59, s58, 0x80
	ds_read_b128 v[170:173], v137 offset:49152
	ds_read_b128 v[174:177], v137 offset:50176
	ds_read_b128 v[178:181], v137 offset:51200
	ds_read_b128 v[182:185], v137 offset:52224
	ds_read_b128 v[186:189], v137 offset:53248
	ds_read_b128 v[190:193], v137 offset:54272
	ds_read_b128 v[194:197], v137 offset:55296
	ds_read_b128 v[198:201], v137 offset:56320
	buffer_load_dwordx4 v128, s[8:11], s59 offen lds
	s_mov_b32 m0, s38
	s_add_i32 s58, s58, 0x80080
	buffer_load_dwordx4 v129, s[8:11], s59 offen lds
	s_mov_b32 m0, s41
	s_bitset1_b32 s57, 7
	buffer_load_dwordx4 v128, s[8:11], s58 offen lds
	s_mov_b32 m0, s42
	s_nop 0
	buffer_load_dwordx4 v129, s[8:11], s58 offen lds
	s_mov_b32 m0, s39
	s_nop 0
	buffer_load_dwordx4 v130, s[4:7], s57 offen lds
	s_mov_b32 m0, s40
	s_nop 0
	buffer_load_dwordx4 v131, s[4:7], s57 offen lds
	s_waitcnt vmcnt(8)
	s_waitcnt lgkmcnt(0)
	s_barrier
	s_setprio 1
	v_mfma_f32_16x16x32_bf16 v[56:59], v[138:141], v[170:173], v[56:59]
	v_mfma_f32_16x16x32_bf16 v[48:51], v[146:149], v[170:173], v[48:51]
	v_mfma_f32_16x16x32_bf16 v[40:43], v[138:141], v[178:181], v[40:43]
	v_mfma_f32_16x16x32_bf16 v[32:35], v[146:149], v[178:181], v[32:35]
	v_mfma_f32_16x16x32_bf16 v[24:27], v[138:141], v[186:189], v[24:27]
	v_mfma_f32_16x16x32_bf16 v[16:19], v[146:149], v[186:189], v[16:19]
	v_mfma_f32_16x16x32_bf16 v[4:7], v[138:141], v[194:197], v[4:7]
	v_mfma_f32_16x16x32_bf16 v[0:3], v[146:149], v[194:197], v[0:3]
	v_mfma_f32_16x16x32_bf16 v[56:59], v[142:145], v[174:177], v[56:59]
	v_mfma_f32_16x16x32_bf16 v[48:51], v[150:153], v[174:177], v[48:51]
	v_mfma_f32_16x16x32_bf16 v[40:43], v[142:145], v[182:185], v[40:43]
	v_mfma_f32_16x16x32_bf16 v[32:35], v[150:153], v[182:185], v[32:35]
	v_mfma_f32_16x16x32_bf16 v[24:27], v[142:145], v[190:193], v[24:27]
	v_mfma_f32_16x16x32_bf16 v[16:19], v[150:153], v[190:193], v[16:19]
	v_mfma_f32_16x16x32_bf16 v[4:7], v[142:145], v[198:201], v[4:7]
	v_mfma_f32_16x16x32_bf16 v[0:3], v[150:153], v[198:201], v[0:3]
	s_setprio 0
	s_setprio 1
	v_mfma_f32_16x16x32_bf16 v[60:63], v[154:157], v[170:173], v[60:63]
	v_mfma_f32_16x16x32_bf16 v[52:55], v[162:165], v[170:173], v[52:55]
	v_mfma_f32_16x16x32_bf16 v[44:47], v[154:157], v[178:181], v[44:47]
	v_mfma_f32_16x16x32_bf16 v[36:39], v[162:165], v[178:181], v[36:39]
	v_mfma_f32_16x16x32_bf16 v[28:31], v[154:157], v[186:189], v[28:31]
	v_mfma_f32_16x16x32_bf16 v[20:23], v[162:165], v[186:189], v[20:23]
	v_mfma_f32_16x16x32_bf16 v[8:11], v[154:157], v[194:197], v[8:11]
	v_mfma_f32_16x16x32_bf16 v[12:15], v[162:165], v[194:197], v[12:15]
	v_mfma_f32_16x16x32_bf16 v[60:63], v[158:161], v[174:177], v[60:63]
	v_mfma_f32_16x16x32_bf16 v[52:55], v[166:169], v[174:177], v[52:55]
	v_mfma_f32_16x16x32_bf16 v[44:47], v[158:161], v[182:185], v[44:47]
	v_mfma_f32_16x16x32_bf16 v[36:39], v[166:169], v[182:185], v[36:39]
	v_mfma_f32_16x16x32_bf16 v[28:31], v[158:161], v[190:193], v[28:31]
	v_mfma_f32_16x16x32_bf16 v[20:23], v[166:169], v[190:193], v[20:23]
	v_mfma_f32_16x16x32_bf16 v[8:11], v[158:161], v[198:201], v[8:11]
	v_mfma_f32_16x16x32_bf16 v[12:15], v[166:169], v[198:201], v[12:15]
	s_setprio 0
	s_barrier
	s_add_i32 s56, s56, 2
	s_addk_i32 s55, 0x100
	s_addk_i32 s54, 0x100
	s_cmp_gt_u32 s56, 29
	s_cbranch_scc0 .LBB0_955
	s_and_b64 vcc, exec, s[16:17]
	s_cbranch_vccz .LBB0_958
	s_barrier

.Lp9_na_done:
	v_add_u32_e32 v133, 0x10000, v169
	v_add_u32_e32 v142, 0x14000, v169
	ds_read_b128 v[134:137], v133
	ds_read_b128 v[138:141], v133 offset:1024
	ds_read_b128 v[176:179], v133 offset:2048
	ds_read_b128 v[180:183], v133 offset:3072
	ds_read_b128 v[184:187], v142
	ds_read_b128 v[188:191], v142 offset:1024
	ds_read_b128 v[192:195], v142 offset:2048
	ds_read_b128 v[196:199], v142 offset:3072
	s_add_i32 s70, s66, s68
	s_add_i32 s71, s68, 0xffffff80
	s_cmp_eq_u32 s67, 12
	s_cselect_b64 vcc, -1, 0
	s_and_b64 s[10:11], vcc, exec
	v_cndmask_b32_e32 v133, v129, v147, vcc
	s_cselect_b32 s69, 0, s68
	v_cndmask_b32_e32 v142, v131, v174, vcc
	v_cndmask_b32_e32 v143, v130, v173, vcc
	s_mov_b32 m0, s43
	ds_read_b128 v[200:203], v170
	ds_read_b128 v[204:207], v170 offset:1024
	ds_read_b128 v[208:211], v170 offset:2048
	ds_read_b128 v[212:215], v170 offset:3072
	ds_read_b128 v[216:219], v170 offset:4096
	ds_read_b128 v[220:223], v170 offset:5120
	ds_read_b128 v[224:227], v170 offset:6144
	ds_read_b128 v[228:231], v170 offset:7168
	buffer_load_dwordx4 v131, s[4:7], s71 offen lds
	s_mov_b32 m0, s44
	s_cselect_b32 s70, s23, s70
	buffer_load_dwordx4 v132, s[4:7], s71 offen lds
	s_waitcnt vmcnt(8)
	s_waitcnt lgkmcnt(0)
	s_barrier
	s_setprio 1
	v_mfma_f32_16x16x128_f8f6f4 v[124:127], v[134:141], v[200:207], v[124:127]
	v_mfma_f32_16x16x128_f8f6f4 v[120:123], v[176:183], v[200:207], v[120:123]
	v_mfma_f32_16x16x128_f8f6f4 v[108:111], v[134:141], v[208:215], v[108:111]
	v_mfma_f32_16x16x128_f8f6f4 v[104:107], v[176:183], v[208:215], v[104:107]
	v_mfma_f32_16x16x128_f8f6f4 v[92:95], v[134:141], v[216:223], v[92:95]
	v_mfma_f32_16x16x128_f8f6f4 v[88:91], v[176:183], v[216:223], v[88:91]
	v_mfma_f32_16x16x128_f8f6f4 v[76:79], v[134:141], v[224:231], v[76:79]
	v_mfma_f32_16x16x128_f8f6f4 v[72:75], v[176:183], v[224:231], v[72:75]
	s_setprio 0
	s_setprio 1
	v_mfma_f32_16x16x128_f8f6f4 v[116:119], v[184:191], v[200:207], v[116:119]
	v_mfma_f32_16x16x128_f8f6f4 v[112:115], v[192:199], v[200:207], v[112:115]
	v_mfma_f32_16x16x128_f8f6f4 v[100:103], v[184:191], v[208:215], v[100:103]
	v_mfma_f32_16x16x128_f8f6f4 v[96:99], v[192:199], v[208:215], v[96:99]
	v_mfma_f32_16x16x128_f8f6f4 v[84:87], v[184:191], v[216:223], v[84:87]
	v_mfma_f32_16x16x128_f8f6f4 v[80:83], v[192:199], v[216:223], v[80:83]
	v_mfma_f32_16x16x128_f8f6f4 v[68:71], v[184:191], v[224:231], v[68:71]
	v_mfma_f32_16x16x128_f8f6f4 v[64:67], v[192:199], v[224:231], v[64:67]
	s_setprio 0
	s_barrier
	s_mov_b32 m0, s26
	s_mov_b32 s10, s6
	s_mov_b32 s11, s7
	ds_read_b128 v[200:203], v170 offset:16384
	ds_read_b128 v[204:207], v170 offset:17408
	ds_read_b128 v[208:211], v170 offset:18432
	ds_read_b128 v[212:215], v170 offset:19456
	ds_read_b128 v[216:219], v170 offset:20480
	ds_read_b128 v[220:223], v170 offset:21504
	ds_read_b128 v[224:227], v170 offset:22528
	ds_read_b128 v[228:231], v170 offset:23552
	buffer_load_dwordx4 v157, s[8:11], s70 offen lds
	s_mov_b32 m0, s27
	s_add_i32 s71, s70, 0x40000
	buffer_load_dwordx4 v159, s[8:11], s70 offen lds
	s_mov_b32 m0, s28
	s_nop 0
	buffer_load_dwordx4 v157, s[8:11], s71 offen lds
	s_mov_b32 m0, s29
	s_nop 0
	buffer_load_dwordx4 v159, s[8:11], s71 offen lds
	s_mov_b32 m0, s25
	s_nop 0
	buffer_load_dwordx4 v133, s[4:7], s69 offen lds
	s_mov_b32 m0, s30
	s_nop 0
	buffer_load_dwordx4 v143, s[4:7], s69 offen lds
	s_waitcnt vmcnt(8)
	s_waitcnt lgkmcnt(0)
	s_barrier
	s_setprio 1
	v_mfma_f32_16x16x128_f8f6f4 v[60:63], v[134:141], v[200:207], v[60:63]
	v_mfma_f32_16x16x128_f8f6f4 v[56:59], v[176:183], v[200:207], v[56:59]
	v_mfma_f32_16x16x128_f8f6f4 v[44:47], v[134:141], v[208:215], v[44:47]
	v_mfma_f32_16x16x128_f8f6f4 v[40:43], v[176:183], v[208:215], v[40:43]
	v_mfma_f32_16x16x128_f8f6f4 v[28:31], v[134:141], v[216:223], v[28:31]
	v_mfma_f32_16x16x128_f8f6f4 v[24:27], v[176:183], v[216:223], v[24:27]
	v_mfma_f32_16x16x128_f8f6f4 v[12:15], v[134:141], v[224:231], v[12:15]
	v_mfma_f32_16x16x128_f8f6f4 v[8:11], v[176:183], v[224:231], v[8:11]
	s_setprio 0
	s_setprio 1
	v_mfma_f32_16x16x128_f8f6f4 v[52:55], v[184:191], v[200:207], v[52:55]
	v_mfma_f32_16x16x128_f8f6f4 v[48:51], v[192:199], v[200:207], v[48:51]
	v_mfma_f32_16x16x128_f8f6f4 v[36:39], v[184:191], v[208:215], v[36:39]
	v_mfma_f32_16x16x128_f8f6f4 v[32:35], v[192:199], v[208:215], v[32:35]
	v_mfma_f32_16x16x128_f8f6f4 v[20:23], v[184:191], v[216:223], v[20:23]
	v_mfma_f32_16x16x128_f8f6f4 v[16:19], v[192:199], v[216:223], v[16:19]
	v_mfma_f32_16x16x128_f8f6f4 v[4:7], v[184:191], v[224:231], v[4:7]
	v_mfma_f32_16x16x128_f8f6f4 v[0:3], v[192:199], v[224:231], v[0:3]
	s_setprio 0
	s_barrier
	v_add_u32_e32 v144, 0x18000, v169
	ds_read_b128 v[134:137], v144
	ds_read_b128 v[138:141], v144 offset:1024
	ds_read_b128 v[176:179], v144 offset:2048
	ds_read_b128 v[180:183], v144 offset:3072
	v_add_u32_e32 v144, 0x1c000, v169
	ds_read_b128 v[184:187], v144
	ds_read_b128 v[188:191], v144 offset:1024
	ds_read_b128 v[192:195], v144 offset:2048
	ds_read_b128 v[196:199], v144 offset:3072
	s_mov_b32 m0, s31
	ds_read_b128 v[200:203], v170 offset:32768
	ds_read_b128 v[204:207], v170 offset:33792
	ds_read_b128 v[208:211], v170 offset:34816
	ds_read_b128 v[212:215], v170 offset:35840
	ds_read_b128 v[216:219], v170 offset:36864
	ds_read_b128 v[220:223], v170 offset:37888
	ds_read_b128 v[224:227], v170 offset:38912
	ds_read_b128 v[228:231], v170 offset:39936
	v_cndmask_b32_e32 v144, v132, v175, vcc
	buffer_load_dwordx4 v142, s[4:7], s69 offen lds
	s_mov_b32 m0, s33
	s_nop 0
	buffer_load_dwordx4 v144, s[4:7], s69 offen lds
	s_waitcnt vmcnt(8)
	s_waitcnt lgkmcnt(0)
	s_barrier
	s_setprio 1
	v_mfma_f32_16x16x128_f8f6f4 v[124:127], v[134:141], v[200:207], v[124:127]
	v_mfma_f32_16x16x128_f8f6f4 v[120:123], v[176:183], v[200:207], v[120:123]
	v_mfma_f32_16x16x128_f8f6f4 v[108:111], v[134:141], v[208:215], v[108:111]
	v_mfma_f32_16x16x128_f8f6f4 v[104:107], v[176:183], v[208:215], v[104:107]
	v_mfma_f32_16x16x128_f8f6f4 v[92:95], v[134:141], v[216:223], v[92:95]
	v_mfma_f32_16x16x128_f8f6f4 v[88:91], v[176:183], v[216:223], v[88:91]
	v_mfma_f32_16x16x128_f8f6f4 v[76:79], v[134:141], v[224:231], v[76:79]
	v_mfma_f32_16x16x128_f8f6f4 v[72:75], v[176:183], v[224:231], v[72:75]
	s_setprio 0
	s_setprio 1
	v_mfma_f32_16x16x128_f8f6f4 v[116:119], v[184:191], v[200:207], v[116:119]
	v_mfma_f32_16x16x128_f8f6f4 v[112:115], v[192:199], v[200:207], v[112:115]
	v_mfma_f32_16x16x128_f8f6f4 v[100:103], v[184:191], v[208:215], v[100:103]
	v_mfma_f32_16x16x128_f8f6f4 v[96:99], v[192:199], v[208:215], v[96:99]
	v_mfma_f32_16x16x128_f8f6f4 v[84:87], v[184:191], v[216:223], v[84:87]
	v_mfma_f32_16x16x128_f8f6f4 v[80:83], v[192:199], v[216:223], v[80:83]
	v_mfma_f32_16x16x128_f8f6f4 v[68:71], v[184:191], v[224:231], v[68:71]
	v_mfma_f32_16x16x128_f8f6f4 v[64:67], v[192:199], v[224:231], v[64:67]
	s_setprio 0
	s_barrier
	s_mov_b32 m0, s35
	s_add_i32 s71, s70, 0x80
	ds_read_b128 v[200:203], v170 offset:49152
	ds_read_b128 v[204:207], v170 offset:50176
	ds_read_b128 v[208:211], v170 offset:51200
	ds_read_b128 v[212:215], v170 offset:52224
	ds_read_b128 v[216:219], v170 offset:53248
	ds_read_b128 v[220:223], v170 offset:54272
	ds_read_b128 v[224:227], v170 offset:55296
	ds_read_b128 v[228:231], v170 offset:56320
	buffer_load_dwordx4 v157, s[8:11], s71 offen lds
	s_mov_b32 m0, s36
	s_add_i32 s70, s70, 0x40080
	buffer_load_dwordx4 v159, s[8:11], s71 offen lds
	s_mov_b32 m0, s41
	s_bitset1_b32 s69, 7
	buffer_load_dwordx4 v157, s[8:11], s70 offen lds
	s_mov_b32 m0, s42
	s_nop 0
	buffer_load_dwordx4 v159, s[8:11], s70 offen lds
	s_mov_b32 m0, s37
	s_nop 0
	buffer_load_dwordx4 v133, s[4:7], s69 offen lds
	s_mov_b32 m0, s40
	s_nop 0
	buffer_load_dwordx4 v143, s[4:7], s69 offen lds
	s_waitcnt vmcnt(8)
	s_waitcnt lgkmcnt(0)
	s_barrier
	s_setprio 1
	v_mfma_f32_16x16x128_f8f6f4 v[60:63], v[134:141], v[200:207], v[60:63]
	v_mfma_f32_16x16x128_f8f6f4 v[56:59], v[176:183], v[200:207], v[56:59]
	v_mfma_f32_16x16x128_f8f6f4 v[44:47], v[134:141], v[208:215], v[44:47]
	v_mfma_f32_16x16x128_f8f6f4 v[40:43], v[176:183], v[208:215], v[40:43]
	v_mfma_f32_16x16x128_f8f6f4 v[28:31], v[134:141], v[216:223], v[28:31]
	v_mfma_f32_16x16x128_f8f6f4 v[24:27], v[176:183], v[216:223], v[24:27]
	v_mfma_f32_16x16x128_f8f6f4 v[12:15], v[134:141], v[224:231], v[12:15]
	v_mfma_f32_16x16x128_f8f6f4 v[8:11], v[176:183], v[224:231], v[8:11]
	s_setprio 0
	s_setprio 1
	v_mfma_f32_16x16x128_f8f6f4 v[52:55], v[184:191], v[200:207], v[52:55]
	v_mfma_f32_16x16x128_f8f6f4 v[48:51], v[192:199], v[200:207], v[48:51]
	v_mfma_f32_16x16x128_f8f6f4 v[36:39], v[184:191], v[208:215], v[36:39]
	v_mfma_f32_16x16x128_f8f6f4 v[32:35], v[192:199], v[208:215], v[32:35]
	v_mfma_f32_16x16x128_f8f6f4 v[20:23], v[184:191], v[216:223], v[20:23]
	v_mfma_f32_16x16x128_f8f6f4 v[16:19], v[192:199], v[216:223], v[16:19]
	v_mfma_f32_16x16x128_f8f6f4 v[4:7], v[184:191], v[224:231], v[4:7]
	v_mfma_f32_16x16x128_f8f6f4 v[0:3], v[192:199], v[224:231], v[0:3]
	s_setprio 0
	s_barrier
	s_add_i32 s67, s67, 2
	s_addk_i32 s68, 0x100
	s_cmp_gt_u32 s67, 13
	s_cbranch_scc0 .LBB0_1157
	s_and_b64 vcc, exec, s[18:19]
	s_cbranch_vccz .LBB0_1160
	s_barrier

.LBB0_1254:
	v_add_u32_e32 v140, 0x10000, v177
	v_add_u32_e32 v141, 0x14000, v177
	ds_read_b128 v[132:135], v140
	ds_read_b128 v[136:139], v140 offset:1024
	ds_read_b128 v[186:189], v140 offset:2048
	ds_read_b128 v[190:193], v140 offset:3072
	ds_read_b128 v[194:197], v141
	ds_read_b128 v[198:201], v141 offset:1024
	ds_read_b128 v[202:205], v141 offset:2048
	ds_read_b128 v[206:209], v141 offset:3072
	s_add_i32 s10, s6, s5
	s_add_i32 s11, s5, 0xffffff80
	s_cmp_eq_u32 s4, 12
	s_cselect_b64 vcc, -1, 0
	s_and_b64 s[8:9], vcc, exec
	v_cndmask_b32_e32 v140, v128, v182, vcc
	s_cselect_b32 s7, 0, s5
	v_cndmask_b32_e32 v141, v130, v184, vcc
	v_cndmask_b32_e32 v142, v129, v183, vcc
	s_mov_b32 m0, s57
	ds_read_b128 v[210:213], v178
	ds_read_b128 v[214:217], v178 offset:1024
	ds_read_b128 v[218:221], v178 offset:2048
	ds_read_b128 v[222:225], v178 offset:3072
	ds_read_b128 v[226:229], v178 offset:4096
	ds_read_b128 v[230:233], v178 offset:5120
	ds_read_b128 v[234:237], v178 offset:6144
	ds_read_b128 v[238:241], v178 offset:7168
	buffer_load_dwordx4 v130, s[20:23], s11 offen lds
	s_mov_b32 m0, s58
	s_cselect_b32 s8, s80, s10
	buffer_load_dwordx4 v131, s[20:23], s11 offen lds
	s_waitcnt vmcnt(8)
	s_waitcnt lgkmcnt(0)
	s_barrier
	s_setprio 1
	v_mfma_f32_16x16x128_f8f6f4 v[124:127], v[132:139], v[210:217], v[124:127]
	v_mfma_f32_16x16x128_f8f6f4 v[120:123], v[186:193], v[210:217], v[120:123]
	v_mfma_f32_16x16x128_f8f6f4 v[108:111], v[132:139], v[218:225], v[108:111]
	v_mfma_f32_16x16x128_f8f6f4 v[104:107], v[186:193], v[218:225], v[104:107]
	v_mfma_f32_16x16x128_f8f6f4 v[92:95], v[132:139], v[226:233], v[92:95]
	v_mfma_f32_16x16x128_f8f6f4 v[88:91], v[186:193], v[226:233], v[88:91]
	v_mfma_f32_16x16x128_f8f6f4 v[76:79], v[132:139], v[234:241], v[76:79]
	v_mfma_f32_16x16x128_f8f6f4 v[72:75], v[186:193], v[234:241], v[72:75]
	s_setprio 0
	s_setprio 1
	v_mfma_f32_16x16x128_f8f6f4 v[116:119], v[194:201], v[210:217], v[116:119]
	v_mfma_f32_16x16x128_f8f6f4 v[112:115], v[202:209], v[210:217], v[112:115]
	v_mfma_f32_16x16x128_f8f6f4 v[100:103], v[194:201], v[218:225], v[100:103]
	v_mfma_f32_16x16x128_f8f6f4 v[96:99], v[202:209], v[218:225], v[96:99]
	v_mfma_f32_16x16x128_f8f6f4 v[84:87], v[194:201], v[226:233], v[84:87]
	v_mfma_f32_16x16x128_f8f6f4 v[80:83], v[202:209], v[226:233], v[80:83]
	v_mfma_f32_16x16x128_f8f6f4 v[68:71], v[194:201], v[234:241], v[68:71]
	v_mfma_f32_16x16x128_f8f6f4 v[64:67], v[202:209], v[234:241], v[64:67]
	s_setprio 0
	s_barrier
	s_mov_b32 m0, s43
	s_mov_b32 s26, s22
	s_mov_b32 s27, s23
	ds_read_b128 v[210:213], v178 offset:16384
	ds_read_b128 v[214:217], v178 offset:17408
	ds_read_b128 v[218:221], v178 offset:18432
	ds_read_b128 v[222:225], v178 offset:19456
	ds_read_b128 v[226:229], v178 offset:20480
	ds_read_b128 v[230:233], v178 offset:21504
	ds_read_b128 v[234:237], v178 offset:22528
	ds_read_b128 v[238:241], v178 offset:23552
	buffer_load_dwordx4 v155, s[24:27], s8 offen lds
	s_mov_b32 m0, s44
	s_add_i32 s9, s8, 0x40000
	buffer_load_dwordx4 v161, s[24:27], s8 offen lds
	s_mov_b32 m0, s45
	s_nop 0
	buffer_load_dwordx4 v155, s[24:27], s9 offen lds
	s_mov_b32 m0, s46
	s_nop 0
	buffer_load_dwordx4 v161, s[24:27], s9 offen lds
	s_mov_b32 m0, s42
	s_nop 0
	buffer_load_dwordx4 v140, s[20:23], s7 offen lds
	s_mov_b32 m0, s47
	s_nop 0
	buffer_load_dwordx4 v142, s[20:23], s7 offen lds
	s_waitcnt vmcnt(8)
	s_waitcnt lgkmcnt(0)
	s_barrier
	s_setprio 1
	v_mfma_f32_16x16x128_f8f6f4 v[60:63], v[132:139], v[210:217], v[60:63]
	v_mfma_f32_16x16x128_f8f6f4 v[56:59], v[186:193], v[210:217], v[56:59]
	v_mfma_f32_16x16x128_f8f6f4 v[44:47], v[132:139], v[218:225], v[44:47]
	v_mfma_f32_16x16x128_f8f6f4 v[40:43], v[186:193], v[218:225], v[40:43]
	v_mfma_f32_16x16x128_f8f6f4 v[28:31], v[132:139], v[226:233], v[28:31]
	v_mfma_f32_16x16x128_f8f6f4 v[24:27], v[186:193], v[226:233], v[24:27]
	v_mfma_f32_16x16x128_f8f6f4 v[12:15], v[132:139], v[234:241], v[12:15]
	v_mfma_f32_16x16x128_f8f6f4 v[8:11], v[186:193], v[234:241], v[8:11]
	s_setprio 0
	s_setprio 1
	v_mfma_f32_16x16x128_f8f6f4 v[52:55], v[194:201], v[210:217], v[52:55]
	v_mfma_f32_16x16x128_f8f6f4 v[48:51], v[202:209], v[210:217], v[48:51]
	v_mfma_f32_16x16x128_f8f6f4 v[36:39], v[194:201], v[218:225], v[36:39]
	v_mfma_f32_16x16x128_f8f6f4 v[32:35], v[202:209], v[218:225], v[32:35]
	v_mfma_f32_16x16x128_f8f6f4 v[20:23], v[194:201], v[226:233], v[20:23]
	v_mfma_f32_16x16x128_f8f6f4 v[16:19], v[202:209], v[226:233], v[16:19]
	v_mfma_f32_16x16x128_f8f6f4 v[4:7], v[194:201], v[234:241], v[4:7]
	v_mfma_f32_16x16x128_f8f6f4 v[0:3], v[202:209], v[234:241], v[0:3]
	s_setprio 0
	s_barrier
	v_add_u32_e32 v143, 0x18000, v177
	ds_read_b128 v[132:135], v143
	ds_read_b128 v[136:139], v143 offset:1024
	ds_read_b128 v[186:189], v143 offset:2048
	ds_read_b128 v[190:193], v143 offset:3072
	v_add_u32_e32 v143, 0x1c000, v177
	ds_read_b128 v[194:197], v143
	ds_read_b128 v[198:201], v143 offset:1024
	ds_read_b128 v[202:205], v143 offset:2048
	ds_read_b128 v[206:209], v143 offset:3072
	s_mov_b32 m0, s48
	ds_read_b128 v[210:213], v178 offset:32768
	ds_read_b128 v[214:217], v178 offset:33792
	ds_read_b128 v[218:221], v178 offset:34816
	ds_read_b128 v[222:225], v178 offset:35840
	ds_read_b128 v[226:229], v178 offset:36864
	ds_read_b128 v[230:233], v178 offset:37888
	ds_read_b128 v[234:237], v178 offset:38912
	ds_read_b128 v[238:241], v178 offset:39936
	v_cndmask_b32_e32 v143, v131, v185, vcc
	buffer_load_dwordx4 v141, s[20:23], s7 offen lds
	s_mov_b32 m0, s49
	s_nop 0
	buffer_load_dwordx4 v143, s[20:23], s7 offen lds
	s_waitcnt vmcnt(8)
	s_waitcnt lgkmcnt(0)
	s_barrier
	s_setprio 1
	v_mfma_f32_16x16x128_f8f6f4 v[124:127], v[132:139], v[210:217], v[124:127]
	v_mfma_f32_16x16x128_f8f6f4 v[120:123], v[186:193], v[210:217], v[120:123]
	v_mfma_f32_16x16x128_f8f6f4 v[108:111], v[132:139], v[218:225], v[108:111]
	v_mfma_f32_16x16x128_f8f6f4 v[104:107], v[186:193], v[218:225], v[104:107]
	v_mfma_f32_16x16x128_f8f6f4 v[92:95], v[132:139], v[226:233], v[92:95]
	v_mfma_f32_16x16x128_f8f6f4 v[88:91], v[186:193], v[226:233], v[88:91]
	v_mfma_f32_16x16x128_f8f6f4 v[76:79], v[132:139], v[234:241], v[76:79]
	v_mfma_f32_16x16x128_f8f6f4 v[72:75], v[186:193], v[234:241], v[72:75]
	s_setprio 0
	s_setprio 1
	v_mfma_f32_16x16x128_f8f6f4 v[116:119], v[194:201], v[210:217], v[116:119]
	v_mfma_f32_16x16x128_f8f6f4 v[112:115], v[202:209], v[210:217], v[112:115]
	v_mfma_f32_16x16x128_f8f6f4 v[100:103], v[194:201], v[218:225], v[100:103]
	v_mfma_f32_16x16x128_f8f6f4 v[96:99], v[202:209], v[218:225], v[96:99]
	v_mfma_f32_16x16x128_f8f6f4 v[84:87], v[194:201], v[226:233], v[84:87]
	v_mfma_f32_16x16x128_f8f6f4 v[80:83], v[202:209], v[226:233], v[80:83]
	v_mfma_f32_16x16x128_f8f6f4 v[68:71], v[194:201], v[234:241], v[68:71]
	v_mfma_f32_16x16x128_f8f6f4 v[64:67], v[202:209], v[234:241], v[64:67]
	s_setprio 0
	s_barrier
	s_mov_b32 m0, s51
	s_add_i32 s9, s8, 0x80
	ds_read_b128 v[210:213], v178 offset:49152
	ds_read_b128 v[214:217], v178 offset:50176
	ds_read_b128 v[218:221], v178 offset:51200
	ds_read_b128 v[222:225], v178 offset:52224
	ds_read_b128 v[226:229], v178 offset:53248
	ds_read_b128 v[230:233], v178 offset:54272
	ds_read_b128 v[234:237], v178 offset:55296
	ds_read_b128 v[238:241], v178 offset:56320
	buffer_load_dwordx4 v155, s[24:27], s9 offen lds
	s_mov_b32 m0, s52
	s_add_i32 s8, s8, 0x40080
	buffer_load_dwordx4 v161, s[24:27], s9 offen lds
	s_mov_b32 m0, s55
	s_bitset1_b32 s7, 7
	buffer_load_dwordx4 v155, s[24:27], s8 offen lds
	s_mov_b32 m0, s56
	s_nop 0
	buffer_load_dwordx4 v161, s[24:27], s8 offen lds
	s_mov_b32 m0, s53
	s_nop 0
	buffer_load_dwordx4 v140, s[20:23], s7 offen lds
	s_mov_b32 m0, s54
	s_nop 0
	buffer_load_dwordx4 v142, s[20:23], s7 offen lds
	s_waitcnt vmcnt(8)
	s_waitcnt lgkmcnt(0)
	s_barrier
	s_setprio 1
	v_mfma_f32_16x16x128_f8f6f4 v[60:63], v[132:139], v[210:217], v[60:63]
	v_mfma_f32_16x16x128_f8f6f4 v[56:59], v[186:193], v[210:217], v[56:59]
	v_mfma_f32_16x16x128_f8f6f4 v[44:47], v[132:139], v[218:225], v[44:47]
	v_mfma_f32_16x16x128_f8f6f4 v[40:43], v[186:193], v[218:225], v[40:43]
	v_mfma_f32_16x16x128_f8f6f4 v[28:31], v[132:139], v[226:233], v[28:31]
	v_mfma_f32_16x16x128_f8f6f4 v[24:27], v[186:193], v[226:233], v[24:27]
	v_mfma_f32_16x16x128_f8f6f4 v[12:15], v[132:139], v[234:241], v[12:15]
	v_mfma_f32_16x16x128_f8f6f4 v[8:11], v[186:193], v[234:241], v[8:11]
	s_setprio 0
	s_setprio 1
	v_mfma_f32_16x16x128_f8f6f4 v[52:55], v[194:201], v[210:217], v[52:55]
	v_mfma_f32_16x16x128_f8f6f4 v[48:51], v[202:209], v[210:217], v[48:51]
	v_mfma_f32_16x16x128_f8f6f4 v[36:39], v[194:201], v[218:225], v[36:39]
	v_mfma_f32_16x16x128_f8f6f4 v[32:35], v[202:209], v[218:225], v[32:35]
	v_mfma_f32_16x16x128_f8f6f4 v[20:23], v[194:201], v[226:233], v[20:23]
	v_mfma_f32_16x16x128_f8f6f4 v[16:19], v[202:209], v[226:233], v[16:19]
	v_mfma_f32_16x16x128_f8f6f4 v[4:7], v[194:201], v[234:241], v[4:7]
	v_mfma_f32_16x16x128_f8f6f4 v[0:3], v[202:209], v[234:241], v[0:3]
	s_setprio 0
	s_barrier
	s_add_i32 s4, s4, 2
	s_addk_i32 s5, 0x100
	s_cmp_gt_u32 s4, 13
	s_cbranch_scc0 .LBB0_1254
	s_and_b64 vcc, exec, s[38:39]
	s_cbranch_vccz .LBB0_1257
	s_barrier
